# phase-3 address setup (32 VALU/SALU) hoisted into the exp phase's LDS-wait shadow
# baseline (speedup 1.0000x reference)
_Z7na_mainPKDF16_PKhS0_PKfS4_S4_S4_Pf:
	s_lshl_b32 s3, s2, 5
	s_and_b32 s3, s3, 0xe0
	s_ashr_i32 s2, s2, 3
	s_add_i32 s3, s3, s2
	s_ashr_i32 s2, s3, 6
	s_lshl_b32 s3, s3, 5
	s_and_b32 s14, s3, 0x7e0
	v_mov_b32_e32 v1, 0x7c0
	s_load_dwordx8 s[4:11], s[0:1], 0x0
	s_load_dwordx2 s[18:19], s[0:1], 0x20
	s_load_dwordx2 s[28:29], s[0:1], 0x28
	s_load_dwordx2 s[34:35], s[0:1], 0x30
	s_load_dwordx2 s[30:31], s[0:1], 0x38
	v_med3_u32 v1, s14, 32, v1
	v_subrev_u32_e32 v97, 32, v1
	s_ashr_i32 s3, s2, 31
	v_lshlrev_b32_e32 v58, 1, v97
	s_lshl_b64 s[12:13], s[2:3], 12
	v_mov_b32_e32 v59, 0
	v_sub_u32_e32 v60, s14, v97
	v_lshl_add_u64 v[10:11], s[12:13], 0, v[58:59]
	v_lshlrev_b64 v[2:3], 9, v[10:11]
	v_lshl_or_b32 v22, v60, 6, v0
	s_waitcnt lgkmcnt(0)
	s_load_dword s32, s[28:29], 0x0
	v_and_b32_e32 v208, 31, v0
	v_lshlrev_b32_e32 v208, 5, v208
	global_load_dwordx4 v[192:195], v208, s[18:19]
	global_load_dwordx4 v[196:199], v208, s[18:19] offset:16
	v_lshl_add_u64 v[20:21], s[4:5], 0, v[2:3]
	v_ashrrev_i32_e32 v23, 31, v22
	v_lshl_add_u64 v[2:3], v[22:23], 4, v[20:21]
	global_load_dwordx4 v[12:15], v[2:3], off
	v_or_b32_e32 v28, 0x200, v22
	v_ashrrev_i32_e32 v29, 31, v28
	v_lshl_add_u64 v[2:3], v[28:29], 4, v[20:21]
	global_load_dwordx4 v[16:19], v[2:3], off
	v_or_b32_e32 v184, 0x400, v22
	v_ashrrev_i32_e32 v185, 31, v184
	v_lshl_add_u64 v[184:185], v[184:185], 4, v[20:21]
	v_or_b32_e32 v188, 0x600, v22
	v_ashrrev_i32_e32 v189, 31, v188
	v_lshl_add_u64 v[188:189], v[188:189], 4, v[20:21]
	global_load_dwordx4 v[184:187], v[184:185], off
	global_load_dwordx4 v[188:191], v[188:189], off
	v_lshrrev_b32_e32 v99, 6, v0
	v_and_b32_e32 v98, 63, v0
	v_lshlrev_b32_e32 v118, 13, v99
	v_lshl_or_b32 v58, v98, 4, v118
	v_and_b32_e32 v58, 0xfff0, v58
	v_add_u32_e32 v251, 0x1000, v58
	s_movk_i32 s15, 0x1000
	v_lshl_add_u64 v[24:25], s[6:7], 0, v[58:59]
	v_or_b32_e32 v32, 0x400, v22
	v_or_b32_e32 v62, 0x600, v22
	v_add_co_u32_e32 v64, vcc, s15, v24
	s_mov_b64 s[12:13], 0x1000
	s_mov_b64 s[16:17], 0x1800
	v_lshlrev_b32_e32 v72, 1, v60
	v_lshrrev_b32_e32 v23, 5, v22
	v_and_b32_e32 v34, 32, v22
	v_ashrrev_i32_e32 v33, 31, v32
	v_ashrrev_i32_e32 v63, 31, v62
	v_addc_co_u32_e32 v65, vcc, 0, v25, vcc
	global_load_dwordx4 v[6:9], v58, s[6:7] offset:1024
	global_load_dwordx4 v[2:5], v58, s[6:7]
	global_load_dwordx4 v[54:57], v58, s[6:7] offset:3072
	global_load_dwordx4 v[50:53], v58, s[6:7] offset:2048
	v_lshrrev_b32_e32 v58, 6, v22
	v_bfe_u32 v73, v22, 8, 2
	v_lshl_add_u64 v[26:27], v[24:25], 0, s[12:13]
	v_lshl_add_u64 v[24:25], v[24:25], 0, s[16:17]
	v_cmp_ne_u32_e32 vcc, 0, v34
	v_sub_u32_e32 v75, v23, v72
	global_load_dwordx4 v[42:45], v251, s[6:7]
	global_load_dwordx4 v[46:49], v251, s[6:7] offset:1024
	global_load_dwordx4 v[34:37], v251, s[6:7] offset:2048
	global_load_dwordx4 v[38:41], v251, s[6:7] offset:3072
	v_mov_b32_e32 v61, 0x60
	v_cndmask_b32_e32 v74, 0, v61, vcc
	v_add_u32_e32 v33, v74, v58
	v_lshlrev_b32_e32 v64, 2, v33
	v_bfe_u32 v96, v0, 4, 1
	v_and_b32_e32 v100, 15, v0
	v_mov_b32_e32 v30, v59
	v_mov_b32_e32 v31, v59
	v_and_b32_e32 v64, 12, v64
	v_mul_u32_u24_e32 v29, 0xc000, v96
	v_bitop3_b32 v64, v64, v100, v73 bitop3:0x36
	v_lshl_or_b32 v64, v64, 4, v29
	v_lshlrev_b32_e32 v63, 1, v75
	v_lshl_add_u32 v33, v33, 8, v64
	v_bfe_u32 v71, v0, 1, 4
	v_and_b32_e32 v70, 32, v0
	v_lshlrev_b32_e32 v1, 3, v0
	v_lshrrev_b32_e32 v58, 1, v75
	v_and_b32_e32 v1, 8, v1
	v_add_lshl_u32 v58, v58, v70, 8
	v_lshlrev_b32_e32 v121, 3, v99
	v_bfe_u32 v101, v0, 4, 2
	v_lshlrev_b32_e32 v102, 2, v101
	v_and_b32_e32 v116, 31, v0
	v_bfe_u32 v119, v0, 5, 1
	v_lshlrev_b32_e32 v124, 1, v119
	v_lshlrev_b32_e32 v117, 8, v116
	v_lshrrev_b32_e32 v95, 4, v0
	s_movk_i32 s16, 0x60
	s_mov_b32 s17, 0xc000
	v_and_b32_e32 v211, 3, v99
	v_lshrrev_b32_e32 v212, 2, v99
	v_lshl_or_b32 v211, v211, 2, v212
	v_xor_b32_e32 v213, v100, v211
	v_mul_u32_u24_e32 v214, 0x60, v119
	v_add3_u32 v214, v214, v60, v99
	v_mul_u32_u24_e32 v215, 0xc000, v96
	v_lshl_add_u32 v214, v214, 8, v215
	v_lshl_or_b32 v220, v213, 4, v214
	v_xor_b32_e32 v221, 32, v220
	v_xor_b32_e32 v216, v71, v211
	v_lshl_add_u32 v217, v119, 5, v99
	v_lshlrev_b32_e32 v217, 8, v217
	v_lshl_or_b32 v216, v216, 4, v217
	v_or_b32_e32 v216, v216, v1
	v_add_u32_e32 v222, 0x23800, v216
	v_xor_b32_e32 v223, 32, v222
	s_waitcnt vmcnt(11)
	ds_write_b128 v220, v[12:15]
	v_fma_mix_f32 v200, v192, v12, 0 op_sel_hi:[0,1,0]
	v_fma_mix_f32 v201, v193, v12, 0 op_sel:[0,1,0] op_sel_hi:[0,1,0]
	v_cvt_f32_f16_e32 v211, v12
	v_cvt_f32_f16_sdwa v212, v12 dst_sel:DWORD dst_unused:UNUSED_PAD src0_sel:WORD_1
	v_fma_mix_f32 v200, v194, v13, v200 op_sel_hi:[0,1,0]
	v_fma_mix_f32 v201, v195, v13, v201 op_sel:[0,1,0] op_sel_hi:[0,1,0]
	v_cvt_f32_f16_e32 v213, v13
	v_cvt_f32_f16_sdwa v214, v13 dst_sel:DWORD dst_unused:UNUSED_PAD src0_sel:WORD_1
	v_fma_mix_f32 v200, v196, v14, v200 op_sel_hi:[0,1,0]
	v_fma_mix_f32 v201, v197, v14, v201 op_sel:[0,1,0] op_sel_hi:[0,1,0]
	v_cvt_f32_f16_e32 v215, v14
	v_cvt_f32_f16_sdwa v216, v14 dst_sel:DWORD dst_unused:UNUSED_PAD src0_sel:WORD_1
	v_fma_mix_f32 v200, v198, v15, v200 op_sel_hi:[0,1,0]
	v_fma_mix_f32 v201, v199, v15, v201 op_sel:[0,1,0] op_sel_hi:[0,1,0]
	v_cvt_f32_f16_e32 v217, v15
	v_cvt_f32_f16_sdwa v218, v15 dst_sel:DWORD dst_unused:UNUSED_PAD src0_sel:WORD_1
	v_cvt_pk_fp8_f32 v224, v211, v212
	v_cvt_pk_fp8_f32 v225, v215, v216
	v_cvt_pk_fp8_f32 v224, v213, v214 op_sel:[0,0,1]
	v_cvt_pk_fp8_f32 v225, v217, v218 op_sel:[0,0,1]
	s_nop 0
	ds_write_b64 v222, v[224:225]
	s_waitcnt vmcnt(10)
	ds_write_b128 v221, v[16:19] offset:2048
	v_fma_mix_f32 v202, v192, v16, 0 op_sel_hi:[0,1,0]
	v_fma_mix_f32 v203, v193, v16, 0 op_sel:[0,1,0] op_sel_hi:[0,1,0]
	v_cvt_f32_f16_e32 v211, v16
	v_cvt_f32_f16_sdwa v212, v16 dst_sel:DWORD dst_unused:UNUSED_PAD src0_sel:WORD_1
	v_fma_mix_f32 v202, v194, v17, v202 op_sel_hi:[0,1,0]
	v_fma_mix_f32 v203, v195, v17, v203 op_sel:[0,1,0] op_sel_hi:[0,1,0]
	v_cvt_f32_f16_e32 v213, v17
	v_cvt_f32_f16_sdwa v214, v17 dst_sel:DWORD dst_unused:UNUSED_PAD src0_sel:WORD_1
	v_fma_mix_f32 v202, v196, v18, v202 op_sel_hi:[0,1,0]
	v_fma_mix_f32 v203, v197, v18, v203 op_sel:[0,1,0] op_sel_hi:[0,1,0]
	v_cvt_f32_f16_e32 v215, v18
	v_cvt_f32_f16_sdwa v216, v18 dst_sel:DWORD dst_unused:UNUSED_PAD src0_sel:WORD_1
	v_fma_mix_f32 v202, v198, v19, v202 op_sel_hi:[0,1,0]
	v_fma_mix_f32 v203, v199, v19, v203 op_sel:[0,1,0] op_sel_hi:[0,1,0]
	v_cvt_f32_f16_e32 v217, v19
	v_cvt_f32_f16_sdwa v218, v19 dst_sel:DWORD dst_unused:UNUSED_PAD src0_sel:WORD_1
	v_cvt_pk_fp8_f32 v226, v211, v212
	v_cvt_pk_fp8_f32 v227, v215, v216
	v_cvt_pk_fp8_f32 v226, v213, v214 op_sel:[0,0,1]
	v_cvt_pk_fp8_f32 v227, v217, v218 op_sel:[0,0,1]
	s_nop 0
	ds_write_b64 v223, v[226:227] offset:2048
	s_waitcnt vmcnt(9)
	ds_write_b128 v220, v[184:187] offset:4096
	v_fma_mix_f32 v204, v192, v184, 0 op_sel_hi:[0,1,0]
	v_fma_mix_f32 v205, v193, v184, 0 op_sel:[0,1,0] op_sel_hi:[0,1,0]
	v_cvt_f32_f16_e32 v211, v184
	v_cvt_f32_f16_sdwa v212, v184 dst_sel:DWORD dst_unused:UNUSED_PAD src0_sel:WORD_1
	v_fma_mix_f32 v204, v194, v185, v204 op_sel_hi:[0,1,0]
	v_fma_mix_f32 v205, v195, v185, v205 op_sel:[0,1,0] op_sel_hi:[0,1,0]
	v_cvt_f32_f16_e32 v213, v185
	v_cvt_f32_f16_sdwa v214, v185 dst_sel:DWORD dst_unused:UNUSED_PAD src0_sel:WORD_1
	v_fma_mix_f32 v204, v196, v186, v204 op_sel_hi:[0,1,0]
	v_fma_mix_f32 v205, v197, v186, v205 op_sel:[0,1,0] op_sel_hi:[0,1,0]
	v_cvt_f32_f16_e32 v215, v186
	v_cvt_f32_f16_sdwa v216, v186 dst_sel:DWORD dst_unused:UNUSED_PAD src0_sel:WORD_1
	v_fma_mix_f32 v204, v198, v187, v204 op_sel_hi:[0,1,0]
	v_fma_mix_f32 v205, v199, v187, v205 op_sel:[0,1,0] op_sel_hi:[0,1,0]
	v_cvt_f32_f16_e32 v217, v187
	v_cvt_f32_f16_sdwa v218, v187 dst_sel:DWORD dst_unused:UNUSED_PAD src0_sel:WORD_1
	v_cvt_pk_fp8_f32 v228, v211, v212
	v_cvt_pk_fp8_f32 v229, v215, v216
	v_cvt_pk_fp8_f32 v228, v213, v214 op_sel:[0,0,1]
	v_cvt_pk_fp8_f32 v229, v217, v218 op_sel:[0,0,1]
	s_nop 0
	ds_write_b64 v222, v[228:229] offset:4096
	s_waitcnt vmcnt(8)
	ds_write_b128 v221, v[188:191] offset:6144
	v_fma_mix_f32 v206, v192, v188, 0 op_sel_hi:[0,1,0]
	v_fma_mix_f32 v207, v193, v188, 0 op_sel:[0,1,0] op_sel_hi:[0,1,0]
	v_cvt_f32_f16_e32 v211, v188
	v_cvt_f32_f16_sdwa v212, v188 dst_sel:DWORD dst_unused:UNUSED_PAD src0_sel:WORD_1
	v_fma_mix_f32 v206, v194, v189, v206 op_sel_hi:[0,1,0]
	v_fma_mix_f32 v207, v195, v189, v207 op_sel:[0,1,0] op_sel_hi:[0,1,0]
	v_cvt_f32_f16_e32 v213, v189
	v_cvt_f32_f16_sdwa v214, v189 dst_sel:DWORD dst_unused:UNUSED_PAD src0_sel:WORD_1
	v_fma_mix_f32 v206, v196, v190, v206 op_sel_hi:[0,1,0]
	v_fma_mix_f32 v207, v197, v190, v207 op_sel:[0,1,0] op_sel_hi:[0,1,0]
	v_cvt_f32_f16_e32 v215, v190
	v_cvt_f32_f16_sdwa v216, v190 dst_sel:DWORD dst_unused:UNUSED_PAD src0_sel:WORD_1
	v_fma_mix_f32 v206, v198, v191, v206 op_sel_hi:[0,1,0]
	v_fma_mix_f32 v207, v199, v191, v207 op_sel:[0,1,0] op_sel_hi:[0,1,0]
	v_cvt_f32_f16_e32 v217, v191
	v_cvt_f32_f16_sdwa v218, v191 dst_sel:DWORD dst_unused:UNUSED_PAD src0_sel:WORD_1
	v_cvt_pk_fp8_f32 v230, v211, v212
	v_cvt_pk_fp8_f32 v231, v215, v216
	v_cvt_pk_fp8_f32 v230, v213, v214 op_sel:[0,0,1]
	v_cvt_pk_fp8_f32 v231, v217, v218 op_sel:[0,0,1]
	s_nop 0
	ds_write_b64 v223, v[230:231] offset:6144
	v_add_f32_e32 v200, v200, v201
	v_add_f32_e32 v202, v202, v203
	v_add_f32_e32 v204, v204, v205
	v_add_f32_e32 v206, v206, v207
	v_lshlrev_b32_e32 v208, 7, v119
	v_lshl_add_u32 v208, v99, 2, v208
	v_add_u32_e32 v208, 0x27800, v208
	v_add_f32_dpp v200, v200, v200 quad_perm:[1,0,3,2] row_mask:0xf bank_mask:0xf
	v_add_f32_dpp v202, v202, v202 quad_perm:[1,0,3,2] row_mask:0xf bank_mask:0xf
	v_add_f32_dpp v204, v204, v204 quad_perm:[1,0,3,2] row_mask:0xf bank_mask:0xf
	v_add_f32_dpp v206, v206, v206 quad_perm:[1,0,3,2] row_mask:0xf bank_mask:0xf
	v_add_f32_dpp v200, v200, v200 quad_perm:[2,3,0,1] row_mask:0xf bank_mask:0xf
	v_add_f32_dpp v202, v202, v202 quad_perm:[2,3,0,1] row_mask:0xf bank_mask:0xf
	v_add_f32_dpp v204, v204, v204 quad_perm:[2,3,0,1] row_mask:0xf bank_mask:0xf
	v_add_f32_dpp v206, v206, v206 quad_perm:[2,3,0,1] row_mask:0xf bank_mask:0xf
	v_add_f32_dpp v200, v200, v200 row_half_mirror row_mask:0xf bank_mask:0xf
	v_add_f32_dpp v202, v202, v202 row_half_mirror row_mask:0xf bank_mask:0xf
	v_add_f32_dpp v204, v204, v204 row_half_mirror row_mask:0xf bank_mask:0xf
	v_add_f32_dpp v206, v206, v206 row_half_mirror row_mask:0xf bank_mask:0xf
	v_add_f32_dpp v200, v200, v200 row_mirror row_mask:0xf bank_mask:0xf
	v_add_f32_dpp v202, v202, v202 row_mirror row_mask:0xf bank_mask:0xf
	v_add_f32_dpp v204, v204, v204 row_mirror row_mask:0xf bank_mask:0xf
	v_add_f32_dpp v206, v206, v206 row_mirror row_mask:0xf bank_mask:0xf
	v_add_f32_dpp v200, v200, v200 row_bcast:15 row_mask:0xa bank_mask:0xf
	v_add_f32_dpp v202, v202, v202 row_bcast:15 row_mask:0xa bank_mask:0xf
	v_add_f32_dpp v204, v204, v204 row_bcast:15 row_mask:0xa bank_mask:0xf
	v_add_f32_dpp v206, v206, v206 row_bcast:15 row_mask:0xa bank_mask:0xf
	s_mov_b32 exec_lo, 0xffff0000
	s_mov_b32 exec_hi, 0xffff0000
	ds_write_b32 v208, v200
	ds_write_b32 v208, v202 offset:32
	ds_write_b32 v208, v204 offset:64
	ds_write_b32 v208, v206 offset:96
	s_mov_b64 exec, -1
	v_lshlrev_b32_e32 v201, 7, v99
	v_lshl_or_b32 v201, v119, 4, v201
	global_load_dwordx4 v[184:187], v201, s[10:11]
	global_load_dwordx4 v[188:191], v201, s[10:11] offset:32
	global_load_dwordx4 v[192:195], v201, s[10:11] offset:64
	global_load_dwordx4 v[196:199], v201, s[10:11] offset:96
	v_cmp_lt_i32_e32 vcc, v121, v60
	s_nop 0
	v_mov_b32_e32 v15, v59
	v_cndmask_b32_e64 v12, 32, 0, vcc
	v_add_u32_e32 v16, v12, v121
	v_or_b32_e32 v12, v16, v101
	v_lshlrev_b32_e32 v58, 1, v12
	v_lshrrev_b32_e32 v12, 5, v0
	v_and_b32_e32 v12, 2, v12
	v_bitop3_b32 v14, v102, v100, v12 bitop3:0x36
	v_lshl_add_u64 v[12:13], v[10:11], 0, v[58:59]
	v_lshlrev_b64 v[12:13], 9, v[12:13]
	v_lshlrev_b32_e32 v16, 8, v16
	v_lshl_add_u64 v[12:13], s[4:5], 0, v[12:13]
	v_lshlrev_b32_e32 v14, 4, v14
	v_readfirstlane_b32 s6, v16
	v_add_u32_e32 v17, 0xc000, v16
	v_lshl_add_u64 v[12:13], v[12:13], 0, v[14:15]
	s_mov_b32 m0, s6
	s_mov_b64 s[6:7], 0x100
	v_readfirstlane_b32 s12, v17
	global_load_lds_dwordx4 v[12:13], off
	v_lshl_add_u64 v[12:13], v[12:13], 0, s[6:7]
	s_mov_b32 m0, s12
	v_or_b32_e32 v58, 1, v58
	global_load_lds_dwordx4 v[12:13], off
	v_lshl_add_u64 v[12:13], v[10:11], 0, v[58:59]
	v_lshlrev_b64 v[12:13], 9, v[12:13]
	v_lshl_add_u64 v[12:13], s[4:5], 0, v[12:13]
	v_lshl_add_u64 v[12:13], v[12:13], 0, v[14:15]
	v_add_u32_e32 v14, 0x6000, v16
	v_bfe_u32 v61, v0, 2, 2
	v_readfirstlane_b32 s12, v14
	v_add_u32_e32 v14, 0x12000, v16
	s_mov_b32 m0, s12
	v_readfirstlane_b32 s12, v14
	global_load_lds_dwordx4 v[12:13], off
	v_lshl_add_u64 v[12:13], v[12:13], 0, s[6:7]
	s_mov_b32 m0, s12
	v_add_u32_e32 v18, 0x23800, v117
	global_load_lds_dwordx4 v[12:13], off
	v_or_b32_e32 v12, 4, v121
	v_cmp_lt_i32_e32 vcc, v12, v60
	s_nop 1
	v_cndmask_b32_e64 v13, 32, 0, vcc
	v_add_u32_e32 v16, v13, v12
	v_or_b32_e32 v13, v16, v101
	v_lshlrev_b32_e32 v58, 1, v13
	v_bfe_u32 v12, v12, 2, 2
	v_bitop3_b32 v14, v102, v100, v12 bitop3:0x36
	v_lshl_add_u64 v[12:13], v[10:11], 0, v[58:59]
	v_lshlrev_b64 v[12:13], 9, v[12:13]
	v_lshlrev_b32_e32 v16, 8, v16
	v_lshl_add_u64 v[12:13], s[4:5], 0, v[12:13]
	v_lshlrev_b32_e32 v14, 4, v14
	v_readfirstlane_b32 s12, v16
	v_add_u32_e32 v17, 0xc000, v16
	v_lshl_add_u64 v[12:13], v[12:13], 0, v[14:15]
	s_mov_b32 m0, s12
	v_readfirstlane_b32 s12, v17
	v_or_b32_e32 v58, 1, v58
	global_load_lds_dwordx4 v[12:13], off
	v_lshl_add_u64 v[12:13], v[12:13], 0, s[6:7]
	s_mov_b32 m0, s12
	v_lshl_add_u64 v[10:11], v[10:11], 0, v[58:59]
	global_load_lds_dwordx4 v[12:13], off
	v_lshlrev_b64 v[10:11], 9, v[10:11]
	v_add_u32_e32 v12, 0x6000, v16
	v_lshl_add_u64 v[10:11], s[4:5], 0, v[10:11]
	v_readfirstlane_b32 s4, v12
	v_add_u32_e32 v12, 0x12000, v16
	v_lshl_add_u64 v[10:11], v[10:11], 0, v[14:15]
	s_mov_b32 m0, s4
	v_readfirstlane_b32 s4, v12
	global_load_lds_dwordx4 v[10:11], off
	v_lshl_add_u64 v[10:11], v[10:11], 0, s[6:7]
	s_mov_b32 m0, s4
	s_nop 0
	global_load_lds_dwordx4 v[10:11], off
	s_waitcnt lgkmcnt(0)
	s_barrier
	v_lshlrev_b32_e32 v10, 2, v0
	v_and_b32_e32 v94, 12, v10
	v_or_b32_e32 v120, v94, v61
	v_bitop3_b32 v10, v124, v94, v61 bitop3:0x1e
	v_lshl_or_b32 v14, v10, 4, v18
	v_bitop3_b32 v10, v124, v120, 1 bitop3:0x36
	v_lshl_or_b32 v19, v10, 4, v18
	ds_read_b128 v[10:13], v14
	ds_read_b128 v[62:65], v14 offset:8192
	ds_read_b128 v[14:17], v19
	ds_read_b128 v[66:69], v19 offset:8192
	v_bitop3_b32 v19, v124, v120, 4 bitop3:0x36
	v_lshl_or_b32 v19, v19, 4, v18
	v_bitop3_b32 v20, v124, v120, 5 bitop3:0x36
	v_lshl_or_b32 v20, v20, 4, v18
	ds_read_b128 v[70:73], v19
	ds_read_b128 v[78:81], v19 offset:8192
	ds_read_b128 v[74:77], v20
	ds_read_b128 v[82:85], v20 offset:8192
	v_bitop3_b32 v19, v124, v120, 8 bitop3:0x36
	v_lshl_or_b32 v19, v19, 4, v18
	v_bitop3_b32 v20, v124, v120, 9 bitop3:0x36
	v_lshl_or_b32 v20, v20, 4, v18
	ds_read_b128 v[86:89], v19
	ds_read_b128 v[104:107], v19 offset:8192
	ds_read_b128 v[90:93], v20
	ds_read_b128 v[108:111], v20 offset:8192
	v_bitop3_b32 v19, v124, v120, 12 bitop3:0x36
	v_lshl_or_b32 v19, v19, 4, v18
	v_bitop3_b32 v20, v124, v120, 13 bitop3:0x36
	v_lshl_or_b32 v18, v20, 4, v18
	ds_read_b128 v[126:129], v19
	ds_read_b128 v[134:137], v19 offset:8192
	ds_read_b128 v[130:133], v18
	ds_read_b128 v[138:141], v18 offset:8192
	v_mov_b32_e32 v103, 0x7f
	v_lshlrev_b32_e32 v58, 7, v99
	v_or_b32_e32 v122, 0x18000, v117
	s_waitcnt vmcnt(18) lgkmcnt(0)
	v_mfma_scale_f32_32x32x64_f8f6f4 v[18:33], v[2:9], v[10:17], 0, v103, v103 op_sel_hi:[0,0,0]
	v_lshlrev_b32_e32 v125, 3, v119
	v_or_b32_e32 v123, 0x1a000, v117
	v_mfma_scale_f32_32x32x64_f8f6f4 v[2:17], v[2:9], v[62:69], 0, v103, v103 op_sel_hi:[0,0,0]
	v_and_b32_e32 v62, 12, v95
	s_waitcnt vmcnt(16)
	v_mfma_scale_f32_32x32x64_f8f6f4 v[18:33], v[50:57], v[70:77], v[18:33], v103, v103 op_sel_hi:[0,0,0]
	v_mfma_scale_f32_32x32x64_f8f6f4 v[2:17], v[50:57], v[78:85], v[2:17], v103, v103 op_sel_hi:[0,0,0]
	s_brev_b32 s10, 60
	v_lshlrev_b32_e32 v58, 6, v0
	v_and_b32_e32 v58, 0x4000, v58
	v_or3_b32 v63, v122, v58, v125
	v_or3_b32 v58, v123, v58, v125
	s_waitcnt vmcnt(14)
	v_mfma_scale_f32_32x32x64_f8f6f4 v[18:33], v[42:49], v[86:93], v[18:33], v103, v103 op_sel_hi:[0,0,0]
	v_mfma_scale_f32_32x32x64_f8f6f4 v[2:17], v[42:49], v[104:111], v[2:17], v103, v103 op_sel_hi:[0,0,0]
	s_nop 0
	s_waitcnt vmcnt(12)
	v_mfma_scale_f32_32x32x64_f8f6f4 v[2:17], v[34:41], v[134:141], v[2:17], v103, v103 op_sel_hi:[0,0,0]
	v_mfma_scale_f32_32x32x64_f8f6f4 v[18:33], v[34:41], v[126:133], v[18:33], v103, v103 op_sel_hi:[0,0,0]
	s_waitcnt vmcnt(8)
	s_nop 15
	s_nop 1
	v_fma_f32 v2, v2, s10, v184
	v_fma_f32 v3, v3, s10, v185
	v_fma_f32 v4, v4, s10, v186
	v_fma_f32 v5, v5, s10, v187
	v_cvt_pk_f16_f32 v2, v2, v3
	v_cvt_pk_f16_f32 v3, v4, v5
	v_bitop3_b32 v4, v95, v120, 12 bitop3:0x6c
	v_pk_fma_f32 v[18:19], v[18:19], s[10:11], v[184:185] op_sel_hi:[1,0,1]
	v_pk_fma_f32 v[20:21], v[20:21], s[10:11], v[186:187] op_sel_hi:[1,0,1]
	v_lshlrev_b32_e32 v4, 4, v4
	v_cvt_pk_f16_f32 v18, v18, v19
	v_cvt_pk_f16_f32 v19, v20, v21
	v_or_b32_e32 v5, v63, v4
	v_or_b32_e32 v4, v58, v4
	ds_write_b64 v5, v[18:19]
	ds_write_b64 v4, v[2:3]
	v_pk_fma_f32 v[2:3], v[22:23], s[10:11], v[188:189] op_sel_hi:[1,0,1]
	v_pk_fma_f32 v[4:5], v[6:7], s[10:11], v[188:189] op_sel_hi:[1,0,1]
	v_pk_fma_f32 v[6:7], v[24:25], s[10:11], v[190:191] op_sel_hi:[1,0,1]
	v_cvt_pk_f16_f32 v2, v2, v3
	v_cvt_pk_f16_f32 v3, v6, v7
	v_pk_fma_f32 v[6:7], v[8:9], s[10:11], v[190:191] op_sel_hi:[1,0,1]
	v_cvt_pk_f16_f32 v4, v4, v5
	v_cvt_pk_f16_f32 v5, v6, v7
	v_bitop3_b32 v6, v62, v120, 1 bitop3:0x36
	v_lshlrev_b32_e32 v6, 4, v6
	v_or_b32_e32 v7, v63, v6
	ds_write_b64 v7, v[2:3]
	v_or_b32_e32 v2, v58, v6
	ds_write_b64 v2, v[4:5]
	v_pk_fma_f32 v[2:3], v[26:27], s[10:11], v[192:193] op_sel_hi:[1,0,1]
	v_pk_fma_f32 v[6:7], v[28:29], s[10:11], v[194:195] op_sel_hi:[1,0,1]
	v_cvt_pk_f16_f32 v2, v2, v3
	v_pk_fma_f32 v[4:5], v[10:11], s[10:11], v[192:193] op_sel_hi:[1,0,1]
	v_cvt_pk_f16_f32 v3, v6, v7
	v_pk_fma_f32 v[6:7], v[12:13], s[10:11], v[194:195] op_sel_hi:[1,0,1]
	v_cvt_pk_f16_f32 v4, v4, v5
	v_cvt_pk_f16_f32 v5, v6, v7
	v_bitop3_b32 v6, v62, v120, 2 bitop3:0x36
	v_lshlrev_b32_e32 v6, 4, v6
	v_or_b32_e32 v7, v63, v6
	ds_write_b64 v7, v[2:3]
	v_or_b32_e32 v2, v58, v6
	ds_write_b64 v2, v[4:5]
	v_pk_fma_f32 v[2:3], v[30:31], s[10:11], v[196:197] op_sel_hi:[1,0,1]
	v_pk_fma_f32 v[6:7], v[32:33], s[10:11], v[198:199] op_sel_hi:[1,0,1]
	v_cvt_pk_f16_f32 v2, v2, v3
	v_pk_fma_f32 v[4:5], v[14:15], s[10:11], v[196:197] op_sel_hi:[1,0,1]
	v_cvt_pk_f16_f32 v3, v6, v7
	v_pk_fma_f32 v[6:7], v[16:17], s[10:11], v[198:199] op_sel_hi:[1,0,1]
	v_cvt_pk_f16_f32 v4, v4, v5
	v_cvt_pk_f16_f32 v5, v6, v7
	v_bitop3_b32 v6, v62, v120, 3 bitop3:0x36
	v_lshlrev_b32_e32 v6, 4, v6
	v_or_b32_e32 v7, v63, v6
	ds_write_b64 v7, v[2:3]
	v_or_b32_e32 v2, v58, v6
	ds_write_b64 v2, v[4:5]
	s_waitcnt vmcnt(0) lgkmcnt(0)
	s_barrier
	v_and_b32_e32 v236, 1, v101
	v_lshrrev_b32_e32 v237, 1, v101
	v_xor_b32_e32 v237, v237, v236
	v_lshl_or_b32 v236, v236, 1, v237
	v_lshrrev_b32_e32 v27, 8, v0
	v_lshrrev_b32_e32 v3, 3, v0
	v_and_b32_e32 v3, 16, v3
	v_mul_u32_u24_e32 v28, 0x60, v27
	v_lshlrev_b32_e32 v26, 5, v27
	v_or_b32_e32 v146, v3, v100
	v_or_b32_e32 v147, v28, v100
	v_or_b32_e32 v4, v146, v26
	v_lshlrev_b32_e32 v209, 2, v4
	v_add_u32_e32 v209, 0x27800, v209
	v_lshlrev_b32_e32 v4, 8, v4
	v_or_b32_e32 v5, 0x18000, v4
	v_bitop3_b32 v11, v236, v120, 12 bitop3:0x36
	v_or_b32_e32 v95, 0x1c000, v4
	v_lshlrev_b32_e32 v29, 3, v101
	v_bitop3_b32 v6, v236, v94, v61 bitop3:0x1e
	v_bitop3_b32 v8, v236, v120, 4 bitop3:0x36
	v_bitop3_b32 v10, v236, v120, 8 bitop3:0x36
	v_lshlrev_b32_e32 v94, 4, v11
	v_lshlrev_b32_e32 v6, 4, v6
	v_lshlrev_b32_e32 v8, 4, v8
	v_lshlrev_b32_e32 v58, 4, v10
	v_or_b32_e32 v7, v5, v6
	v_or_b32_e32 v9, v5, v8
	v_or_b32_e32 v10, v5, v58
	v_or_b32_e32 v5, v5, v94
	v_or_b32_e32 v6, v95, v6
	v_or_b32_e32 v60, v95, v8
	ds_read_b128 v[22:25], v7
	ds_read_b128 v[18:21], v9
	ds_read_b128 v[14:17], v10
	ds_read_b128 v[10:13], v5
	ds_read_b128 v[6:9], v6
	ds_read_b128 v[2:5], v60
	v_bfe_u32 v103, v0, 6, 1
	s_movk_i32 s5, 0x2000
	v_mad_u32_u24 v44, v103, 48, v147
	v_lshlrev_b32_e32 v60, 8, v44
	v_lshlrev_b32_e32 v44, 2, v44
	v_or_b32_e32 v35, v95, v58
	v_lshlrev_b32_e32 v58, 14, v99
	v_and_b32_e32 v44, 12, v44
	v_or_b32_e32 v56, v44, v61
	v_bitop3_b32 v44, v236, v44, v61 bitop3:0x1e
	v_lshl_add_u64 v[32:33], s[8:9], 0, v[58:59]
	v_lshlrev_b32_e32 v58, 4, v98
	v_or_b32_e32 v36, v95, v94
	v_lshl_add_u64 v[88:89], v[32:33], 0, v[58:59]
	v_lshl_or_b32 v57, v44, 4, v60
	ds_read_b128 v[40:43], v35
	ds_read_b128 v[106:109], v36
	global_load_dwordx4 v[36:39], v[88:89], off
	global_load_dwordx4 v[32:35], v[88:89], off offset:1024
	ds_read_b128 v[44:47], v57
	v_bitop3_b32 v48, v236, v56, 4 bitop3:0x36
	v_lshl_or_b32 v62, v48, 4, v60
	ds_read_b128 v[48:51], v62
	v_bitop3_b32 v52, v236, v56, 8 bitop3:0x36
	v_lshl_or_b32 v63, v52, 4, v60
	ds_read_b128 v[52:55], v63
	s_waitcnt lgkmcnt(0)
	v_mfma_f32_16x16x32_f16 v[44:47], v[44:47], v[22:25], 0
	v_bitop3_b32 v64, v236, v56, 12 bitop3:0x36
	ds_read_b128 v[56:59], v57 offset:49152
	v_lshl_or_b32 v60, v64, 4, v60
	v_mfma_f32_16x16x32_f16 v[44:47], v[48:51], v[18:21], v[44:47]
	ds_read_b128 v[68:71], v60
	ds_read_b128 v[72:75], v62 offset:49152
	v_mad_u32_u24 v104, v103, 3, 1
	v_lshlrev_b32_e32 v132, 4, v104
	v_mfma_f32_16x16x32_f16 v[44:47], v[52:55], v[14:17], v[44:47]
	v_add_u32_e32 v52, v132, v147
	global_load_dwordx4 v[64:67], v[88:89], off offset:2048
	global_load_dwordx4 v[48:51], v[88:89], off offset:3072
	ds_read_b128 v[76:79], v63 offset:49152
	ds_read_b128 v[80:83], v60 offset:49152
	s_waitcnt lgkmcnt(3)
	v_mfma_f32_16x16x32_f16 v[44:47], v[68:71], v[10:13], v[44:47]
	v_lshlrev_b32_e32 v60, 8, v52
	v_lshlrev_b32_e32 v52, 2, v52
	v_and_b32_e32 v52, 12, v52
	v_mfma_f32_16x16x32_f16 v[44:47], v[56:59], v[6:9], v[44:47]
	v_or_b32_e32 v62, v52, v61
	v_bitop3_b32 v52, v236, v52, v61 bitop3:0x1e
	v_lshl_or_b32 v63, v52, 4, v60
	s_waitcnt lgkmcnt(2)
	v_mfma_f32_16x16x32_f16 v[44:47], v[72:75], v[2:5], v[44:47]
	ds_read_b128 v[52:55], v63
	v_bitop3_b32 v56, v236, v62, 4 bitop3:0x36
	v_lshl_or_b32 v84, v56, 4, v60
	s_waitcnt lgkmcnt(2)
	v_mfma_f32_16x16x32_f16 v[44:47], v[76:79], v[40:43], v[44:47]
	ds_read_b128 v[56:59], v84
	v_bitop3_b32 v68, v236, v62, 8 bitop3:0x36
	v_lshl_or_b32 v85, v68, 4, v60
	s_waitcnt lgkmcnt(2)
	v_mfma_f32_16x16x32_f16 v[110:113], v[80:83], v[106:109], v[44:47]
	ds_read_b128 v[68:71], v63 offset:49152
	v_bitop3_b32 v62, v236, v62, 12 bitop3:0x36
	v_lshl_or_b32 v60, v62, 4, v60
	ds_read_b128 v[44:47], v85
	s_waitcnt lgkmcnt(3)
	v_mfma_f32_16x16x32_f16 v[52:55], v[52:55], v[22:25], 0
	ds_read_b128 v[72:75], v60
	ds_read_b128 v[76:79], v84 offset:49152
	v_mad_u32_u24 v105, v103, 3, 2
	v_lshlrev_b32_e32 v133, 4, v105
	s_waitcnt lgkmcnt(4)
	v_mfma_f32_16x16x32_f16 v[52:55], v[56:59], v[18:21], v[52:55]
	ds_read_b128 v[56:59], v85 offset:49152
	v_add_co_u32_e32 v114, vcc, s15, v88
	s_waitcnt lgkmcnt(3)
	v_mfma_f32_16x16x32_f16 v[44:47], v[44:47], v[14:17], v[52:55]
	v_addc_co_u32_e32 v115, vcc, 0, v89, vcc
	s_waitcnt lgkmcnt(2)
	v_mfma_f32_16x16x32_f16 v[44:47], v[72:75], v[10:13], v[44:47]
	ds_read_b128 v[52:55], v60 offset:49152
	v_add_u32_e32 v60, v133, v147
	v_lshlrev_b32_e32 v72, 8, v60
	v_lshlrev_b32_e32 v60, 2, v60
	v_mfma_f32_16x16x32_f16 v[44:47], v[68:71], v[6:9], v[44:47]
	v_and_b32_e32 v60, 12, v60
	v_or_b32_e32 v68, v60, v61
	v_bitop3_b32 v60, v236, v60, v61 bitop3:0x1e
	v_lshl_or_b32 v69, v60, 4, v72
	s_waitcnt lgkmcnt(2)
	v_mfma_f32_16x16x32_f16 v[44:47], v[76:79], v[2:5], v[44:47]
	ds_read_b128 v[60:63], v69
	v_bitop3_b32 v70, v236, v68, 4 bitop3:0x36
	v_lshl_or_b32 v70, v70, 4, v72
	s_waitcnt lgkmcnt(2)
	v_mfma_f32_16x16x32_f16 v[44:47], v[56:59], v[40:43], v[44:47]
	ds_read_b128 v[56:59], v70
	v_bitop3_b32 v71, v236, v68, 8 bitop3:0x36
	v_lshl_or_b32 v71, v71, 4, v72
	s_waitcnt lgkmcnt(1)
	v_mfma_f32_16x16x32_f16 v[22:25], v[60:63], v[22:25], 0
	v_bitop3_b32 v60, v236, v68, 12 bitop3:0x36
	v_lshl_or_b32 v68, v60, 4, v72
	ds_read_b32 v210, v209
	v_mfma_f32_16x16x32_f16 v[126:129], v[52:55], v[106:109], v[44:47]
	s_nop 2
	ds_read_b128 v[44:47], v71
	ds_read_b128 v[52:55], v69 offset:49152
	ds_read_b128 v[60:63], v70 offset:49152
	s_waitcnt lgkmcnt(4)
	v_mfma_f32_16x16x32_f16 v[18:21], v[56:59], v[18:21], v[22:25]
	ds_read_b128 v[56:59], v71 offset:49152
	s_nop 1
	ds_read_b128 v[22:25], v68
	s_waitcnt lgkmcnt(4)
	v_mfma_f32_16x16x32_f16 v[14:17], v[44:47], v[14:17], v[18:21]
	v_add_co_u32_e32 v44, vcc, s5, v88
	s_movk_i32 s5, 0x3000
	s_nop 0
	ds_read_b128 v[18:21], v68 offset:49152
	s_waitcnt lgkmcnt(1)
	v_mfma_f32_16x16x32_f16 v[10:13], v[22:25], v[10:13], v[14:17]
	v_addc_co_u32_e32 v45, vcc, 0, v89, vcc
	global_load_dwordx4 v[84:87], v[114:115], off offset:1024
	global_load_dwordx4 v[80:83], v[114:115], off offset:2048
	global_load_dwordx4 v[92:95], v[44:45], off offset:-4096
	global_load_dwordx4 v[76:79], v[44:45], off
	v_mfma_f32_16x16x32_f16 v[6:9], v[52:55], v[6:9], v[10:13]
	global_load_dwordx4 v[72:75], v[44:45], off offset:1024
	global_load_dwordx4 v[68:71], v[44:45], off offset:2048
	global_load_dwordx4 v[52:55], v[44:45], off offset:3072
	v_mov_b32_e32 v13, 0xff61b1e6
	v_mfma_f32_16x16x32_f16 v[2:5], v[60:63], v[2:5], v[6:9]
	s_nop 2
	v_add_co_u32_e32 v6, vcc, s5, v88
	v_mfma_f32_16x16x32_f16 v[2:5], v[56:59], v[40:43], v[2:5]
	s_nop 0
	v_addc_co_u32_e32 v7, vcc, 0, v89, vcc
	global_load_dwordx4 v[88:91], v[114:115], off offset:3072
	global_load_dwordx4 v[60:63], v[6:7], off
	global_load_dwordx4 v[56:59], v[6:7], off offset:1024
	global_load_dwordx4 v[44:47], v[6:7], off offset:2048
	global_load_dwordx4 v[40:43], v[6:7], off offset:3072
	s_waitcnt lgkmcnt(0)
	v_mfma_f32_16x16x32_f16 v[16:19], v[18:21], v[106:109], v[2:5]
	s_mov_b32 s5, 0xff61b1e6
	s_nop 0
	v_or_b32_e32 v3, s14, v146
	v_mov_b32_e32 v4, 0x7df
	v_med3_u32 v3, v3, 32, v4
	v_or_b32_e32 v4, v97, v102
	v_sub_u32_e32 v3, v4, v3
	v_add_f32_e32 v2, s32, v210
	v_add_u32_e32 v3, 32, v3
	v_mad_u32_u24 v4, v103, 48, v3
	s_movk_i32 s4, 0x41
	v_add_f32_e32 v5, v2, v110
	v_mul_f32_e32 v5, 0x3db8aa3b, v5
	v_cmp_gt_u32_e32 vcc, s4, v4
	v_add_u32_e32 v6, 1, v4
	v_add_f32_e32 v7, v2, v111
	v_cndmask_b32_e32 v5, v13, v5, vcc
	v_mul_f32_e32 v7, 0x3db8aa3b, v7
	v_cmp_gt_u32_e32 vcc, s4, v6
	v_add_u32_e32 v8, 2, v4
	v_add_f32_e32 v9, v2, v112
	v_cndmask_b32_e32 v6, v13, v7, vcc
	v_mul_f32_e32 v9, 0x3db8aa3b, v9
	v_cmp_gt_u32_e32 vcc, s4, v8
	v_add_u32_e32 v4, 3, v4
	v_max3_f32 v7, v5, s5, v6
	v_cndmask_b32_e32 v8, v13, v9, vcc
	v_add_f32_e32 v9, v2, v113
	v_mul_f32_e32 v9, 0x3db8aa3b, v9
	v_cmp_gt_u32_e32 vcc, s4, v4
	v_add_u32_e32 v11, v3, v132
	v_add_f32_e32 v12, v2, v127
	v_cndmask_b32_e32 v10, v13, v9, vcc
	v_max3_f32 v4, v7, v8, v10
	v_add_f32_e32 v7, v2, v126
	v_mul_f32_e32 v7, 0x3db8aa3b, v7
	v_cmp_gt_u32_e32 vcc, s4, v11
	v_add_u32_e32 v9, 1, v11
	v_mul_f32_e32 v12, 0x3db8aa3b, v12
	v_cndmask_b32_e32 v7, v13, v7, vcc
	v_cmp_gt_u32_e32 vcc, s4, v9
	v_add_f32_e32 v14, v2, v128
	v_mul_f32_e32 v14, 0x3db8aa3b, v14
	v_cndmask_b32_e32 v9, v13, v12, vcc
	v_add_u32_e32 v12, 2, v11
	v_cmp_gt_u32_e32 vcc, s4, v12
	v_add_u32_e32 v11, 3, v11
	v_add_u32_e32 v3, v3, v133
	v_cndmask_b32_e32 v12, v13, v14, vcc
	v_add_f32_e32 v14, v2, v129
	v_mul_f32_e32 v14, 0x3db8aa3b, v14
	v_cmp_gt_u32_e32 vcc, s4, v11
	v_add_f32_e32 v11, v2, v16
	v_mul_f32_e32 v11, 0x3db8aa3b, v11
	v_cndmask_b32_e32 v15, v13, v14, vcc
	v_cmp_gt_u32_e32 vcc, s4, v3
	v_add_u32_e32 v14, 1, v3
	v_add_f32_e32 v16, v2, v17
	v_cndmask_b32_e32 v11, v13, v11, vcc
	v_mul_f32_e32 v16, 0x3db8aa3b, v16
	v_cmp_gt_u32_e32 vcc, s4, v14
	v_add_f32_e32 v17, v2, v18
	v_max3_f32 v4, v4, v7, v9
	v_cndmask_b32_e32 v14, v13, v16, vcc
	v_add_u32_e32 v16, 2, v3
	v_mul_f32_e32 v17, 0x3db8aa3b, v17
	v_cmp_gt_u32_e32 vcc, s4, v16
	v_add_u32_e32 v3, 3, v3
	v_add_f32_e32 v2, v2, v19
	v_max3_f32 v4, v4, v12, v15
	v_cndmask_b32_e32 v16, v13, v17, vcc
	v_mul_f32_e32 v2, 0x3db8aa3b, v2
	v_cmp_gt_u32_e32 vcc, s4, v3
	v_max3_f32 v4, v4, v11, v14
	v_lshlrev_b32_e32 v126, 5, v99
	v_cndmask_b32_e32 v17, v13, v2, vcc
	v_max3_f32 v2, v4, v16, v17
	v_mov_b32_e32 v3, v2
	v_lshlrev_b32_e32 v127, 2, v119
	v_lshrrev_b32_e32 v4, 7, v0
	v_cmp_gt_u32_e32 vcc, 16, v98
	v_permlane16_swap_b32_e32 v3, v2
	v_max_f32_e32 v2, v2, v3
	v_mov_b32_e32 v3, v2
	s_nop 1
	v_permlane32_swap_b32_e32 v3, v2
	v_max_f32_e32 v13, v2, v3
	v_and_b32_e32 v2, 0x180, v0
	v_or_b32_e32 v2, 0x23400, v2
	v_lshlrev_b32_e32 v3, 2, v100
	s_and_saveexec_b64 s[4:5], vcc
	v_lshlrev_b32_e32 v18, 6, v103
	v_add3_u32 v18, v2, v18, v3
	ds_write_b32 v18, v13
	s_or_b64 exec, exec, s[4:5]
	v_lshlrev_b32_e32 v18, 4, v103
	v_bitop3_b32 v19, v18, 16, v100 bitop3:0x36
	v_lshl_add_u32 v2, v19, 2, v2
	s_waitcnt lgkmcnt(0)
	s_barrier
	ds_read_b32 v19, v2
	v_and_b32_e32 v245, 15, v116
	v_lshrrev_b32_e32 v246, 4, v116
	v_lshl_or_b32 v246, v119, 1, v246
	v_lshrrev_b32_e32 v250, 5, v126
	v_and_b32_e32 v250, 7, v250
	v_and_b32_e32 v247, 1, v246
	v_lshrrev_b32_e32 v248, 1, v246
	v_xor_b32_e32 v248, v248, v247
	v_lshl_or_b32 v247, v247, 1, v248
	v_and_b32_e32 v248, 3, v245
	v_lshrrev_b32_e32 v249, 2, v245
	v_lshl_or_b32 v248, v248, 2, v249
	v_xor_b32_e32 v247, v247, v248
	v_lshlrev_b32_e32 v240, 8, v245
	v_lshl_or_b32 v240, v247, 4, v240
	v_add_u32_e32 v240, 0x18000, v240
	v_xor_b32_e32 v241, 64, v240
	v_xor_b32_e32 v242, 0x80, v240
	v_xor_b32_e32 v243, 0xc0, v240
	v_lshlrev_b32_e32 v249, 7, v250
	v_lshl_or_b32 v249, v246, 4, v249
	v_and_b32_e32 v249, 0x3f0, v249
	v_lshlrev_b32_e32 v244, 19, v250
	v_lshl_or_b32 v244, v246, 16, v244
	v_lshl_or_b32 v244, v245, 3, v244
	v_and_b32_e32 v244, 0x3fff78, v244
	s_lshl_b64 s[22:23], s[2:3], 22
	s_add_u32 s22, s22, s30
	s_addc_u32 s23, s23, s31
	s_lshl_b32 s24, s14, 3
	s_add_u32 s22, s22, s24
	s_addc_u32 s23, s23, 0
	v_max_f32_e32 v13, v13, v13
	v_mul_u32_u24_e32 v20, 0xd00, v4
	v_or_b32_e32 v2, 1, v124
	s_waitcnt lgkmcnt(0)
	v_max_f32_e32 v19, v19, v19
	v_max_f32_e32 v19, v13, v19
	v_sub_f32_e32 v5, v5, v19
	v_exp_f32_e32 v5, v5
	v_sub_f32_e32 v6, v6, v19
	v_exp_f32_e32 v6, v6
	v_sub_f32_e32 v8, v8, v19
	v_mul_u32_u24_e32 v13, 0xd0, v100
	v_exp_f32_e32 v8, v8
	v_sub_f32_e32 v10, v10, v19
	v_add3_u32 v20, v13, v20, v29
	v_exp_f32_e32 v10, v10
	v_or_b32_e32 v22, 0x20000, v20
	v_add_f32_e32 v20, 0, v5
	v_add_f32_e32 v20, v20, v6
	v_add_f32_e32 v20, v20, v8
	v_add_f32_e32 v23, v20, v10
	v_cvt_pk_f16_f32 v21, v8, v10
	v_cvt_pk_f16_f32 v20, v5, v6
	v_mad_u32_u24 v5, v103, s16, v22
	ds_write_b64 v5, v[20:21]
	v_sub_f32_e32 v5, v7, v19
	v_exp_f32_e32 v5, v5
	v_sub_f32_e32 v6, v9, v19
	v_exp_f32_e32 v6, v6
	v_sub_f32_e32 v7, v12, v19
	v_exp_f32_e32 v7, v7
	v_sub_f32_e32 v8, v15, v19
	v_exp_f32_e32 v8, v8
	v_sub_f32_e32 v10, v11, v19
	v_add_f32_e32 v9, v23, v5
	v_exp_f32_e32 v10, v10
	v_sub_f32_e32 v11, v14, v19
	v_add_f32_e32 v9, v9, v6
	v_exp_f32_e32 v11, v11
	v_sub_f32_e32 v12, v16, v19
	v_add_f32_e32 v9, v9, v7
	v_exp_f32_e32 v12, v12
	v_sub_f32_e32 v14, v17, v19
	v_add_f32_e32 v9, v9, v8
	v_exp_f32_e32 v14, v14
	v_add_f32_e32 v9, v9, v10
	v_add_f32_e32 v9, v9, v11
	v_add_f32_e32 v9, v9, v12
	v_add_f32_e32 v9, v9, v14
	v_mov_b32_e32 v15, v9
	v_cvt_pk_f16_f32 v7, v7, v8
	v_cvt_pk_f16_f32 v6, v5, v6
	v_lshl_add_u32 v5, v104, 5, v22
	ds_write_b64 v5, v[6:7]
	v_permlane16_swap_b32_e32 v15, v9
	v_add_f32_e32 v5, v9, v15
	v_mov_b32_e32 v6, v5
	s_movk_i32 s7, 0xd00
	s_mov_b32 s6, 0x20000
	v_cvt_pk_f16_f32 v9, v12, v14
	v_cvt_pk_f16_f32 v8, v10, v11
	v_lshl_add_u32 v7, v105, 5, v22
	ds_write_b64 v7, v[8:9]
	v_permlane32_swap_b32_e32 v6, v5
	s_and_saveexec_b64 s[4:5], vcc
	s_cbranch_execz .LBB1_4
	v_lshlrev_b32_e32 v4, 5, v4
	v_or_b32_e32 v7, v18, v100
	v_lshlrev_b32_e32 v4, 2, v4
	v_lshlrev_b32_e32 v7, 2, v7
	s_mov_b32 s8, 0x23600
	v_add3_u32 v4, v7, v4, s8
	v_add_f32_e32 v5, v5, v6
	ds_write_b32 v4, v5
.LBB1_4:
	s_or_b64 exec, exec, s[4:5]
	v_lshl_or_b32 v4, v27, 1, v96
	v_lshl_or_b32 v3, v4, 7, v3
	v_or_b32_e32 v5, 0x23600, v3
	v_or_b32_e32 v3, 0x23640, v3
	s_waitcnt lgkmcnt(0)
	s_barrier
	ds_read_b32 v5, v5
	ds_read_b32 v3, v3
	v_mad_u32_u24 v4, v4, s7, v13
	v_lshl_add_u32 v4, v119, 4, v4
	v_or_b32_e32 v6, 0x20000, v4
	ds_read_b128 v[16:19], v6
	s_waitcnt lgkmcnt(1)
	v_add_f32_e32 v3, v5, v3
	v_add_u32_e32 v5, 0x20020, v4
	v_add_u32_e32 v6, 0x20040, v4
	ds_read_b128 v[112:115], v5
	ds_read_b128 v[108:111], v6
	v_add_u32_e32 v5, 0x20060, v4
	v_add_u32_e32 v6, 0x20080, v4
	v_lshlrev_b32_e32 v7, 1, v101
	ds_read_b128 v[104:107], v5
	ds_read_b128 v[96:99], v6
	v_lshrrev_b32_e32 v5, 2, v100
	v_or_b32_e32 v6, v28, v125
	v_and_b32_e32 v7, 2, v7
	v_bfe_u32 v8, v0, 1, 1
	v_and_b32_e32 v164, 8, v121
	v_bfe_i32 v9, v0, 7, 1
	v_or3_b32 v8, v8, v7, v164
	v_and_b32_e32 v0, 12, v0
	v_add_lshl_u32 v10, v6, v5, 8
	v_or_b32_e32 v5, v6, v5
	v_and_b32_e32 v9, 0xc000, v9
	v_lshlrev_b32_e32 v12, 8, v5
	v_bitop3_b32 v5, v0, v8, v124 bitop3:0x36
	v_lshl_or_b32 v13, v5, 4, v9
	v_bitop3_b32 v6, v0, v8, v2 bitop3:0x36
	v_or_b32_e32 v15, 0x1000, v12
	v_lshl_or_b32 v14, v6, 4, v9
	v_add_u32_e32 v7, v13, v15
	v_or_b32_e32 v24, 0x1400, v12
	v_or_b32_e32 v20, v7, v1
	v_add_u32_e32 v7, v14, v24
	v_add_u32_e32 v25, 0x2000, v10
	v_add_u32_e32 v5, v13, v12
	v_add_u32_e32 v6, v14, v12
	v_or_b32_e32 v22, v7, v1
	v_add_u32_e32 v7, v13, v25
	v_add_u32_e32 v150, 0x3000, v10
	v_or_b32_e32 v8, 4, v8
	v_add_u32_e32 v4, 0x200a0, v4
	v_or_b32_e32 v5, v5, v1
	v_or_b32_e32 v6, v6, v1
	v_or_b32_e32 v27, v7, v1
	v_add_u32_e32 v31, v13, v150
	v_add_u32_e32 v151, 0x3400, v10
	v_bitop3_b32 v124, v0, v8, v124 bitop3:0x36
	v_bitop3_b32 v0, v0, v8, v2 bitop3:0x36
	ds_read_b128 v[100:103], v4
	ds_read_b64_tr_b16 v[4:5], v5
	ds_read_b64_tr_b16 v[6:7], v6 offset:1024
	ds_read_b64_tr_b16 v[20:21], v20
	ds_read_b64_tr_b16 v[22:23], v22
	ds_read_b64_tr_b16 v[28:29], v27
	v_add_u32_e32 v27, 0x2400, v10
	v_or_b32_e32 v128, v31, v1
	v_add_u32_e32 v31, v14, v151
	v_add_u32_e32 v152, 0x4000, v10
	v_add_u32_e32 v158, 0x4400, v10
	v_lshl_or_b32 v124, v124, 4, v9
	v_lshl_or_b32 v0, v0, 4, v9
	v_add_u32_e32 v11, 0x5000, v10
	v_add_u32_e32 v30, v14, v27
	v_or_b32_e32 v130, v31, v1
	v_add_u32_e32 v31, v13, v152
	v_add_u32_e32 v134, v14, v158
	v_add_u32_e32 v10, 0x5400, v10
	v_add_u32_e32 v135, v124, v12
	v_add_u32_e32 v2, v0, v12
	v_add_u32_e32 v8, v124, v15
	v_or_b32_e32 v30, v30, v1
	v_or_b32_e32 v132, v31, v1
	v_or_b32_e32 v134, v134, v1
	v_add_u32_e32 v13, v13, v11
	v_add_u32_e32 v14, v14, v10
	v_or_b32_e32 v140, v135, v1
	v_or_b32_e32 v2, v2, v1
	v_or_b32_e32 v8, v8, v1
	v_add_u32_e32 v9, v0, v24
	v_add_u32_e32 v12, v124, v25
	ds_read_b64_tr_b16 v[30:31], v30
	ds_read_b64_tr_b16 v[128:129], v128
	ds_read_b64_tr_b16 v[130:131], v130
	ds_read_b64_tr_b16 v[132:133], v132
	v_or_b32_e32 v13, v13, v1
	v_or_b32_e32 v14, v14, v1
	ds_read_b64_tr_b16 v[134:135], v134
	ds_read_b64_tr_b16 v[136:137], v13
	ds_read_b64_tr_b16 v[138:139], v14
	ds_read_b64_tr_b16 v[140:141], v140
	v_or_b32_e32 v9, v9, v1
	v_or_b32_e32 v12, v12, v1
	ds_read_b64_tr_b16 v[142:143], v2 offset:1024
	ds_read_b64_tr_b16 v[144:145], v8
	ds_read_b64_tr_b16 v[146:147], v9
	ds_read_b64_tr_b16 v[148:149], v12
	v_add_u32_e32 v2, v0, v27
	v_add_u32_e32 v8, v124, v150
	v_or_b32_e32 v2, v2, v1
	v_or_b32_e32 v8, v8, v1
	v_add_u32_e32 v9, v0, v151
	v_add_u32_e32 v12, v124, v152
	v_or_b32_e32 v9, v9, v1
	v_or_b32_e32 v12, v12, v1
	ds_read_b64_tr_b16 v[150:151], v2
	ds_read_b64_tr_b16 v[152:153], v8
	ds_read_b64_tr_b16 v[154:155], v9
	ds_read_b64_tr_b16 v[156:157], v12
	v_add_u32_e32 v2, v0, v158
	v_add_u32_e32 v8, v124, v11
	v_add_u32_e32 v0, v0, v10
	v_or_b32_e32 v2, v2, v1
	v_or_b32_e32 v8, v8, v1
	v_or_b32_e32 v0, v0, v1
	v_div_scale_f32 v1, s[8:9], v3, v3, 1.0
	v_rcp_f32_e32 v9, v1
	ds_read_b64_tr_b16 v[158:159], v2
	ds_read_b64_tr_b16 v[160:161], v8
	ds_read_b64_tr_b16 v[162:163], v0
	s_mov_b32 s4, 0xc000
	s_movk_i32 s5, 0x4000
	v_fma_f32 v0, -v1, v9, 1.0
	v_fmac_f32_e32 v9, v0, v9
	v_div_scale_f32 v0, vcc, 1.0, v3, 1.0
	v_mul_f32_e32 v2, v0, v9
	v_fma_f32 v8, -v1, v2, v0
	v_fmac_f32_e32 v2, v8, v9
	v_fma_f32 v0, -v1, v2, v0
	v_div_fmas_f32 v0, v0, v9, v2
	v_div_fixup_f32 v124, v0, v3, 1.0
	s_waitcnt lgkmcnt(14)
	v_mfma_f32_32x32x16_f16 v[0:15], v[4:7], v[16:19], 0
	s_mov_b32 s7, 0x18000
	v_lshlrev_b32_e32 v172, 2, v126
	v_mov_b32_e32 v173, 0
	v_mfma_f32_32x32x16_f16 v[0:15], v[20:23], v[112:115], v[0:15]
	v_or_b32_e32 v20, v26, v116
	v_and_b32_e32 v21, 0x4000, v118
	v_lshl_or_b32 v20, v20, 8, v21
	v_bitop3_b32 v118, v121, v120, 8 bitop3:0x6c
	v_or3_b32 v121, v20, v125, s7
	v_mfma_f32_32x32x16_f16 v[0:15], v[28:31], v[108:111], v[0:15]
	v_mfma_f32_32x32x16_f16 v[0:15], v[128:131], v[104:107], v[0:15]
	v_mfma_f32_32x32x16_f16 v[0:15], v[132:135], v[96:99], v[0:15]
	s_waitcnt lgkmcnt(12)
	v_mfma_f32_32x32x16_f16 v[0:15], v[136:139], v[100:103], v[0:15]
	s_nop 11
	v_fma_mixlo_f16 v20, v124, v0, 0
	v_mov_b32_e32 v0, v1
	v_mov_b32_e32 v1, v2
	v_pk_mul_f32 v[0:1], v[124:125], v[0:1] op_sel_hi:[0,1]
	v_cvt_pk_f16_f32 v1, v0, v1
	v_pack_b32_f16 v0, v20, v1
	s_waitcnt lgkmcnt(10)
	v_mfma_f32_32x32x16_f16 v[16:31], v[140:143], v[16:19], 0
	v_fma_mixlo_f16 v2, v124, v3, 0
	v_alignbit_b32 v1, v2, v1, 16
	v_lshl_or_b32 v2, v118, 4, v121
	ds_write_b64 v2, v[0:1]
	v_mov_b32_e32 v0, v5
	v_mov_b32_e32 v1, v6
	v_pk_mul_f32 v[0:1], v[124:125], v[0:1] op_sel_hi:[0,1]
	s_waitcnt lgkmcnt(9)
	v_mfma_f32_32x32x16_f16 v[16:31], v[144:147], v[112:115], v[16:31]
	v_fma_mixlo_f16 v2, v124, v4, 0
	v_cvt_pk_f16_f32 v1, v0, v1
	v_pack_b32_f16 v0, v2, v1
	v_fma_mixlo_f16 v2, v124, v7, 0
	v_alignbit_b32 v1, v2, v1, 16
	v_bitop3_b32 v2, v164, v120, 1 bitop3:0x36
	v_lshl_or_b32 v2, v2, 4, v121
	s_waitcnt lgkmcnt(7)
	v_mfma_f32_32x32x16_f16 v[16:31], v[148:151], v[108:111], v[16:31]
	ds_write_b64 v2, v[0:1]
	v_mov_b32_e32 v0, v9
	v_mov_b32_e32 v1, v10
	v_mul_f32_e64 v0, v124, v0
	v_mul_f32_e64 v1, v124, v1
	v_fma_mixlo_f16 v2, v124, v8, 0
	v_cvt_pk_f16_f32 v1, v0, v1
	v_pack_b32_f16 v0, v2, v1
	s_waitcnt lgkmcnt(6)
	v_mfma_f32_32x32x16_f16 v[16:31], v[152:155], v[104:107], v[16:31]
	v_fma_mixlo_f16 v2, v124, v11, 0
	v_alignbit_b32 v1, v2, v1, 16
	v_bitop3_b32 v2, v164, v120, 2 bitop3:0x36
	v_lshl_or_b32 v2, v2, 4, v121
	ds_write_b64 v2, v[0:1]
	v_mov_b32_e32 v0, v13
	v_mov_b32_e32 v1, v14
	s_waitcnt lgkmcnt(5)
	v_mfma_f32_32x32x16_f16 v[16:31], v[156:159], v[96:99], v[16:31]
	v_mul_f32_e64 v0, v124, v0
	v_mul_f32_e64 v1, v124, v1
	v_fma_mixlo_f16 v2, v124, v12, 0
	v_cvt_pk_f16_f32 v1, v0, v1
	v_pack_b32_f16 v0, v2, v1
	v_fma_mixlo_f16 v2, v124, v15, 0
	v_alignbit_b32 v1, v2, v1, 16
	v_bitop3_b32 v2, v164, v120, 3 bitop3:0x36
	s_waitcnt lgkmcnt(3)
	v_mfma_f32_32x32x16_f16 v[16:31], v[160:163], v[100:103], v[16:31]
	v_lshl_or_b32 v2, v2, 4, v121
	ds_write_b64 v2, v[0:1]
	s_nop 9
	v_mov_b32_e32 v0, v17
	v_mov_b32_e32 v1, v18
	v_pk_mul_f32 v[0:1], v[124:125], v[0:1] op_sel_hi:[0,1]
	v_fma_mixlo_f16 v2, v124, v16, 0
	v_cvt_pk_f16_f32 v1, v0, v1
	v_pack_b32_f16 v0, v2, v1
	v_fma_mixlo_f16 v2, v124, v19, 0
	v_alignbit_b32 v1, v2, v1, 16
	v_bitop3_b32 v2, v164, v120, 4 bitop3:0x36
	v_lshl_or_b32 v2, v2, 4, v121
	ds_write_b64 v2, v[0:1]
	v_mov_b32_e32 v0, v21
	v_mov_b32_e32 v1, v22
	v_pk_mul_f32 v[0:1], v[124:125], v[0:1] op_sel_hi:[0,1]
	v_fma_mixlo_f16 v2, v124, v20, 0
	v_cvt_pk_f16_f32 v1, v0, v1
	v_pack_b32_f16 v0, v2, v1
	v_fma_mixlo_f16 v2, v124, v23, 0
	v_alignbit_b32 v1, v2, v1, 16
	v_bitop3_b32 v2, v164, v120, 5 bitop3:0x36
	v_lshl_or_b32 v2, v2, 4, v121
	ds_write_b64 v2, v[0:1]
	v_mov_b32_e32 v0, v25
	v_mov_b32_e32 v1, v26
	v_pk_mul_f32 v[0:1], v[124:125], v[0:1] op_sel_hi:[0,1]
	v_fma_mixlo_f16 v2, v124, v24, 0
	v_cvt_pk_f16_f32 v1, v0, v1
	v_pack_b32_f16 v0, v2, v1
	v_fma_mixlo_f16 v2, v124, v27, 0
	v_alignbit_b32 v1, v2, v1, 16
	v_bitop3_b32 v2, v164, v120, 6 bitop3:0x36
	v_lshl_or_b32 v2, v2, 4, v121
	ds_write_b64 v2, v[0:1]
	v_mov_b32_e32 v0, v29
	v_mov_b32_e32 v1, v30
	v_pk_mul_f32 v[0:1], v[124:125], v[0:1] op_sel_hi:[0,1]
	v_fma_mixlo_f16 v2, v124, v28, 0
	v_cvt_pk_f16_f32 v1, v0, v1
	v_pack_b32_f16 v0, v2, v1
	v_fma_mixlo_f16 v2, v124, v31, 0
	v_alignbit_b32 v1, v2, v1, 16
	v_bitop3_b32 v2, v164, v120, 7 bitop3:0x36
	v_lshl_or_b32 v2, v2, 4, v121
	ds_write_b64 v2, v[0:1]
	v_lshl_add_u64 v[0:1], s[0:1], 0, v[172:173]
	v_lshlrev_b32_e32 v172, 2, v127
	v_lshl_add_u64 v[0:1], v[0:1], 0, v[172:173]
	s_waitcnt lgkmcnt(0)
	s_barrier
	global_load_dwordx4 v[96:99], v249, s[34:35]
	global_load_dwordx4 v[100:103], v249, s[34:35] offset:64
	ds_read_b128 v[112:115], v240
	ds_read_b128 v[144:147], v240 offset:8192
	ds_read_b128 v[116:119], v241
	ds_read_b128 v[148:151], v241 offset:8192
	ds_read_b128 v[120:123], v242
	ds_read_b128 v[152:155], v242 offset:8192
	ds_read_b128 v[124:127], v243
	ds_read_b128 v[156:159], v243 offset:8192
	ds_read_b128 v[128:131], v240 offset:16384
	ds_read_b128 v[160:163], v240 offset:24576
	ds_read_b128 v[132:135], v241 offset:16384
	ds_read_b128 v[164:167], v241 offset:24576
	ds_read_b128 v[136:139], v242 offset:16384
	ds_read_b128 v[168:171], v242 offset:24576
	ds_read_b128 v[140:143], v243 offset:16384
	ds_read_b128 v[172:175], v243 offset:24576
	s_waitcnt vmcnt(2)
	s_waitcnt lgkmcnt(14)
	v_mfma_f32_16x16x32_f16 v[0:3], v[36:39], v[112:115], 0
	v_mfma_f32_16x16x32_f16 v[4:7], v[36:39], v[144:147], 0
	v_mfma_f32_16x16x32_f16 v[8:11], v[76:79], v[112:115], 0
	v_mfma_f32_16x16x32_f16 v[12:15], v[76:79], v[144:147], 0
	s_waitcnt lgkmcnt(12)
	v_mfma_f32_16x16x32_f16 v[0:3], v[32:35], v[116:119], v[0:3]
	v_mfma_f32_16x16x32_f16 v[4:7], v[32:35], v[148:151], v[4:7]
	v_mfma_f32_16x16x32_f16 v[8:11], v[72:75], v[116:119], v[8:11]
	v_mfma_f32_16x16x32_f16 v[12:15], v[72:75], v[148:151], v[12:15]
	s_waitcnt lgkmcnt(10)
	v_mfma_f32_16x16x32_f16 v[0:3], v[64:67], v[120:123], v[0:3]
	v_mfma_f32_16x16x32_f16 v[4:7], v[64:67], v[152:155], v[4:7]
	v_mfma_f32_16x16x32_f16 v[8:11], v[68:71], v[120:123], v[8:11]
	v_mfma_f32_16x16x32_f16 v[12:15], v[68:71], v[152:155], v[12:15]
	s_waitcnt lgkmcnt(8)
	v_mfma_f32_16x16x32_f16 v[0:3], v[48:51], v[124:127], v[0:3]
	v_mfma_f32_16x16x32_f16 v[4:7], v[48:51], v[156:159], v[4:7]
	v_mfma_f32_16x16x32_f16 v[8:11], v[52:55], v[124:127], v[8:11]
	v_mfma_f32_16x16x32_f16 v[12:15], v[52:55], v[156:159], v[12:15]
	s_waitcnt lgkmcnt(6)
	v_mfma_f32_16x16x32_f16 v[0:3], v[92:95], v[128:131], v[0:3]
	v_mfma_f32_16x16x32_f16 v[4:7], v[92:95], v[160:163], v[4:7]
	v_mfma_f32_16x16x32_f16 v[8:11], v[60:63], v[128:131], v[8:11]
	v_mfma_f32_16x16x32_f16 v[12:15], v[60:63], v[160:163], v[12:15]
	s_waitcnt lgkmcnt(4)
	v_mfma_f32_16x16x32_f16 v[0:3], v[84:87], v[132:135], v[0:3]
	v_mfma_f32_16x16x32_f16 v[4:7], v[84:87], v[164:167], v[4:7]
	v_mfma_f32_16x16x32_f16 v[8:11], v[56:59], v[132:135], v[8:11]
	v_mfma_f32_16x16x32_f16 v[12:15], v[56:59], v[164:167], v[12:15]
	s_waitcnt lgkmcnt(2)
	v_mfma_f32_16x16x32_f16 v[0:3], v[80:83], v[136:139], v[0:3]
	v_mfma_f32_16x16x32_f16 v[4:7], v[80:83], v[168:171], v[4:7]
	v_mfma_f32_16x16x32_f16 v[8:11], v[44:47], v[136:139], v[8:11]
	v_mfma_f32_16x16x32_f16 v[12:15], v[44:47], v[168:171], v[12:15]
	s_waitcnt lgkmcnt(0)
	v_mfma_f32_16x16x32_f16 v[0:3], v[88:91], v[140:143], v[0:3]
	v_mfma_f32_16x16x32_f16 v[4:7], v[88:91], v[172:175], v[4:7]
	v_mfma_f32_16x16x32_f16 v[8:11], v[40:43], v[140:143], v[8:11]
	v_mfma_f32_16x16x32_f16 v[12:15], v[40:43], v[172:175], v[12:15]
	ds_read_b128 v[176:179], v240 offset:4096
	ds_read_b128 v[208:211], v240 offset:12288
	ds_read_b128 v[180:183], v241 offset:4096
	ds_read_b128 v[212:215], v241 offset:12288
	ds_read_b128 v[184:187], v242 offset:4096
	ds_read_b128 v[216:219], v242 offset:12288
	ds_read_b128 v[188:191], v243 offset:4096
	ds_read_b128 v[220:223], v243 offset:12288
	ds_read_b128 v[192:195], v240 offset:20480
	ds_read_b128 v[224:227], v240 offset:28672
	ds_read_b128 v[196:199], v241 offset:20480
	ds_read_b128 v[228:231], v241 offset:28672
	ds_read_b128 v[200:203], v242 offset:20480
	ds_read_b128 v[232:235], v242 offset:28672
	ds_read_b128 v[204:207], v243 offset:20480
	ds_read_b128 v[236:239], v243 offset:28672
	s_waitcnt vmcnt(0)
	s_waitcnt lgkmcnt(14)
	v_mfma_f32_16x16x32_f16 v[16:19], v[36:39], v[176:179], 0
	v_mfma_f32_16x16x32_f16 v[20:23], v[36:39], v[208:211], 0
	v_mfma_f32_16x16x32_f16 v[24:27], v[76:79], v[176:179], 0
	v_mfma_f32_16x16x32_f16 v[28:31], v[76:79], v[208:211], 0
	s_add_u32 s26, s22, 0x0
	s_addc_u32 s27, s23, 0
	v_add_f32_e32 v104, v0, v96
	v_add_f32_e32 v105, v4, v96
	global_store_dwordx2 v244, v[104:105], s[26:27] nt
	s_waitcnt lgkmcnt(12)
	v_mfma_f32_16x16x32_f16 v[16:19], v[32:35], v[180:183], v[16:19]
	v_mfma_f32_16x16x32_f16 v[20:23], v[32:35], v[212:215], v[20:23]
	v_mfma_f32_16x16x32_f16 v[24:27], v[72:75], v[180:183], v[24:27]
	v_mfma_f32_16x16x32_f16 v[28:31], v[72:75], v[212:215], v[28:31]
	s_add_u32 s26, s22, 0x4000
	s_addc_u32 s27, s23, 0
	v_add_f32_e32 v106, v1, v97
	v_add_f32_e32 v107, v5, v97
	global_store_dwordx2 v244, v[106:107], s[26:27] nt
	s_waitcnt lgkmcnt(10)
	v_mfma_f32_16x16x32_f16 v[16:19], v[64:67], v[184:187], v[16:19]
	v_mfma_f32_16x16x32_f16 v[20:23], v[64:67], v[216:219], v[20:23]
	v_mfma_f32_16x16x32_f16 v[24:27], v[68:71], v[184:187], v[24:27]
	v_mfma_f32_16x16x32_f16 v[28:31], v[68:71], v[216:219], v[28:31]
	s_add_u32 s26, s22, 0x8000
	s_addc_u32 s27, s23, 0
	v_add_f32_e32 v108, v2, v98
	v_add_f32_e32 v109, v6, v98
	global_store_dwordx2 v244, v[108:109], s[26:27] nt
	s_waitcnt lgkmcnt(8)
	v_mfma_f32_16x16x32_f16 v[16:19], v[48:51], v[188:191], v[16:19]
	v_mfma_f32_16x16x32_f16 v[20:23], v[48:51], v[220:223], v[20:23]
	v_mfma_f32_16x16x32_f16 v[24:27], v[52:55], v[188:191], v[24:27]
	v_mfma_f32_16x16x32_f16 v[28:31], v[52:55], v[220:223], v[28:31]
	s_add_u32 s26, s22, 0xc000
	s_addc_u32 s27, s23, 0
	v_add_f32_e32 v110, v3, v99
	v_add_f32_e32 v111, v7, v99
	global_store_dwordx2 v244, v[110:111], s[26:27] nt
	s_waitcnt lgkmcnt(6)
	v_mfma_f32_16x16x32_f16 v[16:19], v[92:95], v[192:195], v[16:19]
	v_mfma_f32_16x16x32_f16 v[20:23], v[92:95], v[224:227], v[20:23]
	v_mfma_f32_16x16x32_f16 v[24:27], v[60:63], v[192:195], v[24:27]
	v_mfma_f32_16x16x32_f16 v[28:31], v[60:63], v[224:227], v[28:31]
	s_add_u32 s26, s22, 0x40000
	s_addc_u32 s27, s23, 0
	v_add_f32_e32 v104, v8, v100
	v_add_f32_e32 v105, v12, v100
	global_store_dwordx2 v244, v[104:105], s[26:27] nt
	s_waitcnt lgkmcnt(4)
	v_mfma_f32_16x16x32_f16 v[16:19], v[84:87], v[196:199], v[16:19]
	v_mfma_f32_16x16x32_f16 v[20:23], v[84:87], v[228:231], v[20:23]
	v_mfma_f32_16x16x32_f16 v[24:27], v[56:59], v[196:199], v[24:27]
	v_mfma_f32_16x16x32_f16 v[28:31], v[56:59], v[228:231], v[28:31]
	s_add_u32 s26, s22, 0x44000
	s_addc_u32 s27, s23, 0
	v_add_f32_e32 v106, v9, v101
	v_add_f32_e32 v107, v13, v101
	global_store_dwordx2 v244, v[106:107], s[26:27] nt
	s_waitcnt lgkmcnt(2)
	v_mfma_f32_16x16x32_f16 v[16:19], v[80:83], v[200:203], v[16:19]
	v_mfma_f32_16x16x32_f16 v[20:23], v[80:83], v[232:235], v[20:23]
	v_mfma_f32_16x16x32_f16 v[24:27], v[44:47], v[200:203], v[24:27]
	v_mfma_f32_16x16x32_f16 v[28:31], v[44:47], v[232:235], v[28:31]
	s_add_u32 s26, s22, 0x48000
	s_addc_u32 s27, s23, 0
	v_add_f32_e32 v108, v10, v102
	v_add_f32_e32 v109, v14, v102
	global_store_dwordx2 v244, v[108:109], s[26:27] nt
	s_waitcnt lgkmcnt(0)
	v_mfma_f32_16x16x32_f16 v[16:19], v[88:91], v[204:207], v[16:19]
	v_mfma_f32_16x16x32_f16 v[20:23], v[88:91], v[236:239], v[20:23]
	v_mfma_f32_16x16x32_f16 v[24:27], v[40:43], v[204:207], v[24:27]
	v_mfma_f32_16x16x32_f16 v[28:31], v[40:43], v[236:239], v[28:31]
	s_add_u32 s26, s22, 0x4c000
	s_addc_u32 s27, s23, 0
	v_add_f32_e32 v110, v11, v103
	v_add_f32_e32 v111, v15, v103
	global_store_dwordx2 v244, v[110:111], s[26:27] nt
	s_nop 7
	s_nop 1
	s_add_u32 s26, s22, 0x0
	s_addc_u32 s27, s23, 0
	v_add_f32_e32 v104, v16, v96
	v_add_f32_e32 v105, v20, v96
	global_store_dwordx2 v244, v[104:105], s[26:27] offset:128 nt
	s_add_u32 s26, s22, 0x4000
	s_addc_u32 s27, s23, 0
	v_add_f32_e32 v106, v17, v97
	v_add_f32_e32 v107, v21, v97
	global_store_dwordx2 v244, v[106:107], s[26:27] offset:128 nt
	s_add_u32 s26, s22, 0x8000
	s_addc_u32 s27, s23, 0
	v_add_f32_e32 v108, v18, v98
	v_add_f32_e32 v109, v22, v98
	global_store_dwordx2 v244, v[108:109], s[26:27] offset:128 nt
	s_add_u32 s26, s22, 0xc000
	s_addc_u32 s27, s23, 0
	v_add_f32_e32 v110, v19, v99
	v_add_f32_e32 v111, v23, v99
	global_store_dwordx2 v244, v[110:111], s[26:27] offset:128 nt
	s_add_u32 s26, s22, 0x40000
	s_addc_u32 s27, s23, 0
	v_add_f32_e32 v104, v24, v100
	v_add_f32_e32 v105, v28, v100
	global_store_dwordx2 v244, v[104:105], s[26:27] offset:128 nt
	s_add_u32 s26, s22, 0x44000
	s_addc_u32 s27, s23, 0
	v_add_f32_e32 v106, v25, v101
	v_add_f32_e32 v107, v29, v101
	global_store_dwordx2 v244, v[106:107], s[26:27] offset:128 nt
	s_add_u32 s26, s22, 0x48000
	s_addc_u32 s27, s23, 0
	v_add_f32_e32 v108, v26, v102
	v_add_f32_e32 v109, v30, v102
	global_store_dwordx2 v244, v[108:109], s[26:27] offset:128 nt
	s_add_u32 s26, s22, 0x4c000
	s_addc_u32 s27, s23, 0
	v_add_f32_e32 v110, v27, v103
	v_add_f32_e32 v111, v31, v103
	global_store_dwordx2 v244, v[110:111], s[26:27] offset:128 nt
	s_endpgm
